# ring-16 hybrid with loads re-issued one at a time (no bursts)
# baseline (speedup 1.0000x reference)
.Lk1_contm_15:
	global_load_dwordx4 v[88:91], v1, s[6:7] nt
	s_add_u32 s6, s6, 0x400
	s_addc_u32 s7, s7, 0
	s_mov_b32 s18, s58
	s_add_u32 s60, s26, 2
	s_cmp_lt_u32 s60, 14
	s_cbranch_scc0 .Lk1_dynid
	s_add_u32 s57, s59, s60
	s_branch .Lk1_haveid
